# band tile-loop cleanup (dead phi copies removed, K/V prefetched directly into operand registers, 32-bit address math) + batched residual loads in out-proj/down epilogues
# speedup vs baseline: 1.0084x; 1.0084x over previous
.LBB0_1259:
	s_cmp_gt_u32 s41, s51
	s_cselect_b64 s[82:83], -1, 0
	s_cmp_le_u32 s41, s51
	s_cselect_b64 s[60:61], -1, 0
	s_mov_b64 s[0:1], -1
	s_and_b64 vcc, exec, s[60:61]
	s_cbranch_vccz .LBB0_1263
	s_andn2_b64 vcc, exec, s[52:53]
	s_cbranch_vccnz .LBB0_1262
	global_load_dwordx4 v[84:87], v[160:161], off
	global_load_dwordx4 v[88:91], v[160:161], off offset:32
	global_load_dwordx4 v[92:95], v[160:161], off offset:64
	global_load_dwordx4 v[96:99], v[160:161], off offset:96
	global_load_dwordx4 v[4:7], v[162:163], off
	global_load_dwordx4 v[8:11], v[162:163], off offset:32
	global_load_dwordx4 v[12:15], v[162:163], off offset:64
	global_load_dwordx4 v[16:19], v[162:163], off offset:96
	global_load_dwordx4 v[68:71], v[164:165], off
	global_load_dwordx4 v[72:75], v[166:167], off
	global_load_dwordx4 v[76:79], v[168:169], off
	global_load_dwordx4 v[80:83], v[170:171], off

.LBB0_1265:
	s_waitcnt vmcnt(0)
	v_mfma_f32_32x32x16_bf16 v[52:67], v[144:147], v[124:127], 0
	ds_write_b128 v191, v[128:131] offset:32768
	ds_write_b128 v191, v[120:123] offset:33280
	ds_write_b128 v191, v[104:107] offset:33792
	ds_write_b128 v191, v[100:103] offset:34304
	ds_read2_b32 v[198:199], v153 offset0:26 offset1:27
	s_andn2_b64 vcc, exec, s[82:83]
	v_mfma_f32_32x32x16_bf16 v[52:67], v[140:143], v[116:119], v[52:67]
	v_mfma_f32_32x32x16_bf16 v[52:67], v[136:139], v[112:115], v[52:67]
	v_mfma_f32_32x32x16_bf16 v[52:67], v[132:135], v[108:111], v[52:67]
	s_cbranch_vccnz .Lband_nopf
	v_mov_b32_e32 v205, 0
	v_lshlrev_b32_e32 v204, s47, v180
	v_add_u32_e32 v204, s56, v204
	v_mul_u32_u24_e32 v204, s5, v204
	v_lshl_add_u64 v[206:207], v[204:205], 0, v[156:157]
	global_load_dwordx4 v[144:147], v[206:207], off
	global_load_dwordx4 v[140:143], v[206:207], off offset:32
	global_load_dwordx4 v[136:139], v[206:207], off offset:64
	global_load_dwordx4 v[132:135], v[206:207], off offset:96
	v_lshlrev_b32_e32 v204, s47, v178
	v_add_u32_e32 v204, s56, v204
	v_mul_u32_u24_e32 v204, s5, v204
	v_lshl_add_u64 v[206:207], v[204:205], 0, v[158:159]
	global_load_dwordx4 v[128:131], v[206:207], off
	v_lshlrev_b32_e32 v204, s47, v176
	v_add_u32_e32 v204, s56, v204
	v_mul_u32_u24_e32 v204, s5, v204
	v_lshl_add_u64 v[206:207], v[204:205], 0, v[158:159]
	global_load_dwordx4 v[120:123], v[206:207], off
	v_lshlrev_b32_e32 v204, s47, v174
	v_add_u32_e32 v204, s56, v204
	v_mul_u32_u24_e32 v204, s5, v204
	v_lshl_add_u64 v[206:207], v[204:205], 0, v[158:159]
	global_load_dwordx4 v[104:107], v[206:207], off
	v_lshlrev_b32_e32 v204, s47, v172
	v_add_u32_e32 v204, s56, v204
	v_mul_u32_u24_e32 v204, s5, v204
	v_lshl_add_u64 v[206:207], v[204:205], 0, v[158:159]
	global_load_dwordx4 v[100:103], v[206:207], off
.Lband_nopf:
	s_waitcnt lgkmcnt(0)
	s_nop 10
	v_fmamk_f32 v197, v52, 0x3e38aa3b, v199
	v_fmac_f32_e32 v198, 0x3e38aa3b, v53
	ds_read2_b32 v[52:53], v153 offset0:24 offset1:25
	v_max3_f32 v195, v197, s33, v198
	s_waitcnt lgkmcnt(0)
	v_fmamk_f32 v53, v54, 0x3e38aa3b, v53
	v_fmac_f32_e32 v52, 0x3e38aa3b, v55
	ds_read2_b32 v[54:55], v153 offset0:18 offset1:19
	v_max3_f32 v195, v195, v53, v52
	s_waitcnt lgkmcnt(0)
	v_fmamk_f32 v55, v56, 0x3e38aa3b, v55
	v_fmac_f32_e32 v54, 0x3e38aa3b, v57
	ds_read2_b32 v[56:57], v153 offset0:16 offset1:17
	v_max3_f32 v195, v195, v55, v54
	s_waitcnt lgkmcnt(0)
	v_fmamk_f32 v57, v58, 0x3e38aa3b, v57
	v_fmac_f32_e32 v56, 0x3e38aa3b, v59
	ds_read2_b32 v[58:59], v153 offset0:10 offset1:11
	v_max3_f32 v195, v195, v57, v56
	s_waitcnt lgkmcnt(0)
	v_fmamk_f32 v59, v60, 0x3e38aa3b, v59
	v_fmac_f32_e32 v58, 0x3e38aa3b, v61
	ds_read2_b32 v[60:61], v153 offset0:8 offset1:9
	v_max3_f32 v195, v195, v59, v58
	s_waitcnt lgkmcnt(0)
	v_fmamk_f32 v61, v62, 0x3e38aa3b, v61
	v_fmac_f32_e32 v60, 0x3e38aa3b, v63
	ds_read2_b32 v[62:63], v153 offset0:2 offset1:3
	v_max3_f32 v195, v195, v61, v60
	s_waitcnt lgkmcnt(0)
	v_fmamk_f32 v63, v64, 0x3e38aa3b, v63
	v_fmac_f32_e32 v62, 0x3e38aa3b, v65
	ds_read2_b32 v[64:65], v153 offset1:1
	v_max3_f32 v195, v195, v63, v62
	s_waitcnt lgkmcnt(0)
	v_fmamk_f32 v65, v66, 0x3e38aa3b, v65
	v_fmac_f32_e32 v64, 0x3e38aa3b, v67
	v_max3_f32 v66, v195, v65, v64
	v_mov_b32_e32 v67, v66
	s_nop 1
	v_permlane32_swap_b32_e32 v66, v67
	v_max3_f32 v195, v196, v66, v67
	v_sub_f32_e32 v67, v197, v195
	v_exp_f32_e32 v67, v67
	v_sub_f32_e32 v197, v198, v195
	v_exp_f32_e32 v197, v197
	v_sub_f32_e32 v53, v53, v195
	v_exp_f32_e32 v53, v53
	v_sub_f32_e32 v52, v52, v195
	v_exp_f32_e32 v52, v52
	v_sub_f32_e32 v55, v55, v195
	v_sub_f32_e32 v66, v196, v195
	v_add_f32_e32 v196, 0, v67
	v_exp_f32_e32 v55, v55
	v_sub_f32_e32 v54, v54, v195
	v_add_f32_e32 v196, v197, v196
	v_exp_f32_e32 v54, v54
	v_sub_f32_e32 v57, v57, v195
	v_add_f32_e32 v196, v53, v196
	v_exp_f32_e32 v198, v57
	v_add_f32_e32 v196, v52, v196
	v_add_f32_e32 v196, v55, v196
	v_add_f32_e32 v196, v54, v196
	v_sub_f32_e32 v56, v56, v195
	v_add_f32_e32 v57, v198, v196
	v_exp_f32_e32 v196, v56
	s_nop 0
	v_add_f32_e32 v56, v196, v57
	v_sub_f32_e32 v57, v59, v195
	v_exp_f32_e32 v59, v57
	v_sub_f32_e32 v57, v58, v195
	v_exp_f32_e32 v199, v57
	v_sub_f32_e32 v57, v61, v195
	v_exp_f32_e32 v200, v57
	v_sub_f32_e32 v57, v60, v195
	v_exp_f32_e32 v201, v57
	v_sub_f32_e32 v57, v63, v195
	v_add_f32_e32 v56, v59, v56
	v_exp_f32_e32 v202, v57
	v_sub_f32_e32 v57, v62, v195
	v_add_f32_e32 v56, v199, v56
	v_exp_f32_e32 v203, v57
	v_sub_f32_e32 v57, v65, v195
	v_add_f32_e32 v56, v200, v56
	v_exp_f32_e32 v65, v57
	v_sub_f32_e32 v57, v64, v195
	v_add_f32_e32 v56, v201, v56
	v_exp_f32_e32 v64, v57
	v_add_f32_e32 v56, v202, v56
	v_add_f32_e32 v56, v203, v56
	v_add_f32_e32 v56, v65, v56
	v_add_f32_e32 v57, v64, v56
	v_exp_f32_e32 v56, v66
	v_cvt_pk_bf16_f32 v60, v67, v197
	v_cvt_pk_bf16_f32 v62, v55, v54
	v_cvt_pk_bf16_f32 v55, v65, v64
	ds_read_b64_tr_b16 v[64:65], v192 offset:32768
	ds_read_b64_tr_b16 v[66:67], v192 offset:33280
	v_mov_b32_e32 v58, v57
	s_nop 1
	v_permlane32_swap_b32_e32 v57, v58
	v_pk_mul_f32 v[34:35], v[34:35], v[56:57] op_sel_hi:[1,0]
	v_pk_mul_f32 v[32:33], v[32:33], v[56:57] op_sel_hi:[1,0]
	v_pk_mul_f32 v[30:31], v[30:31], v[56:57] op_sel_hi:[1,0]
	v_pk_mul_f32 v[28:29], v[28:29], v[56:57] op_sel_hi:[1,0]
	v_pk_mul_f32 v[26:27], v[26:27], v[56:57] op_sel_hi:[1,0]
	v_pk_mul_f32 v[24:25], v[24:25], v[56:57] op_sel_hi:[1,0]
	v_pk_mul_f32 v[22:23], v[22:23], v[56:57] op_sel_hi:[1,0]
	v_pk_mul_f32 v[20:21], v[20:21], v[56:57] op_sel_hi:[1,0]
	v_cvt_pk_bf16_f32 v61, v53, v52
	v_cvt_pk_bf16_f32 v63, v198, v196
	v_cvt_pk_bf16_f32 v52, v59, v199
	v_cvt_pk_bf16_f32 v53, v200, v201
	v_cvt_pk_bf16_f32 v54, v202, v203
	v_pk_mul_f32 v[50:51], v[50:51], v[56:57] op_sel_hi:[1,0]
	s_waitcnt lgkmcnt(0)
	v_mfma_f32_32x32x16_bf16 v[20:35], v[64:67], v[60:63], v[20:35]
	ds_read_b64_tr_b16 v[64:65], v192 offset:33792
	ds_read_b64_tr_b16 v[66:67], v192 offset:34304
	v_mul_f32_e64 v48, v48, v56
	v_mul_f32_e64 v49, v49, v56
	v_mul_f32_e64 v46, v46, v56
	v_mul_f32_e64 v47, v47, v56
	v_pk_mul_f32 v[44:45], v[44:45], v[56:57] op_sel_hi:[1,0]
	v_pk_mul_f32 v[42:43], v[42:43], v[56:57] op_sel_hi:[1,0]
	v_pk_mul_f32 v[40:41], v[40:41], v[56:57] op_sel_hi:[1,0]
	v_pk_mul_f32 v[38:39], v[38:39], v[56:57] op_sel_hi:[1,0]
	s_waitcnt lgkmcnt(0)
	v_mfma_f32_32x32x16_bf16 v[20:35], v[64:67], v[52:55], v[20:35]
	ds_read_b64_tr_b16 v[64:65], v192 offset:34816
	ds_read_b64_tr_b16 v[66:67], v192 offset:35328
	v_mul_f32_e64 v36, v36, v56
	v_mul_f32_e64 v37, v37, v56
	s_waitcnt lgkmcnt(0)
	s_nop 0
	v_mfma_f32_32x32x16_bf16 v[36:51], v[64:67], v[60:63], v[36:51]
	ds_read_b64_tr_b16 v[60:61], v192 offset:35840
	ds_read_b64_tr_b16 v[62:63], v192 offset:36352
	s_waitcnt lgkmcnt(0)
	v_mfma_f32_32x32x16_bf16 v[36:51], v[60:63], v[52:55], v[36:51]
.LBB0_1267:
	v_add_f32_e32 v197, v57, v58
	v_fmac_f32_e32 v197, v194, v56
	s_add_i32 s41, s41, -1
	v_lshl_add_u64 v[172:173], v[172:173], 0, s[96:97]
	v_lshl_add_u64 v[174:175], v[174:175], 0, s[96:97]
	v_lshl_add_u64 v[176:177], v[176:177], 0, s[96:97]
	v_lshl_add_u64 v[178:179], v[178:179], 0, s[96:97]
	v_lshl_add_u64 v[180:181], v[180:181], 0, s[96:97]
	v_add_u32_e32 v153, 0x80, v153
	s_and_b64 vcc, exec, s[60:61]
	s_cbranch_vccnz .LBB0_1269
	v_mov_b32_e32 v196, v195
	v_mov_b32_e32 v194, v197
	s_branch .LBB0_1259
